# P1, P4 and P6 K-loops: all LDS-DMA loads in saddr form (48 v_lshl_add_u64 per 3 loops removed), heads 64B-aligned, on top of combo10
# speedup vs baseline: 1.0090x; 1.0011x over previous
; #define PG8_STAGE(bufoff, gbase, voff) do { _Pragma("unroll") for (int _i = 0; _i < 2; ++_i) \
;         __builtin_amdgcn_global_load_lds((const unsigned*)((const char*)(gbase) + (voff)[_i]), (PG8_LAS unsigned*)(lds + (bufoff) + ldsw + _i * 8192), 16, 0, 0); } while (0)
; #define PG8_LDA(dst, b, h) do { _Pragma("unroll") for (int m = 0; m < 4; ++m) _Pragma("unroll") for (int k = 0; k < 2; ++k) dst[m][k] = *(const PG8_LAS bf16x8*)(lds + PG8_SA(b, h) + aoff + m * 2048 + k * 1024); } while (0)
; #define PG8_LDB(dst, b, h) do { _Pragma("unroll") for (int n = 0; n < 2; ++n) _Pragma("unroll") for (int k = 0; k < 2; ++k) dst[n][k] = *(const PG8_LAS bf16x8*)(lds + PG8_SB(b, h) + boff + n * 2048 + k * 1024); } while (0)
; #define PG8_MMA(ai, bj, At, Bt) do { __builtin_amdgcn_s_setprio(1); _Pragma("unroll") for (int m = 0; m < 4; ++m) _Pragma("unroll") for (int n = 0; n < 2; ++n) _Pragma("unroll") for (int k = 0; k < 2; ++k) \
;         acc[ai][bj][m][n] = __builtin_amdgcn_mfma_f32_16x16x32_bf16(Bt[n][k], At[m][k], acc[ai][bj][m][n], 0, 0, 0); __builtin_amdgcn_s_setprio(0); } while (0)
; #define PG8_WAIT_V(n) asm volatile("s_waitcnt vmcnt(" #n ")" ::: "memory")
; #define PG8_WAIT_L(n) asm volatile("s_waitcnt lgkmcnt(" #n ")" ::: "memory")
; template <class Epi, class Sched, bool ALIGN_EPI = false, bool SP2 = false>
; __device__ __forceinline__ void gemm_phase(PG8_LAS unsigned char* lds, const Gemm g, const Sched& S, const Epi& E) {
;     ...
;             const bool last = (t == nt - 2);
;             const char* a1 = cA + (size_t)(t + 1) * kstep;
;             const char* a2 = last ? nA : cA + (size_t)(t + 2) * kstep; const char* b2 = last ? nB : cB + (size_t)(t + 2) * kstep;
;             const char* a3 = a2 + kstep; const char* b3 = b2 + kstep;
;             if (last && has_next) S.a_ready(nxt);
;             if constexpr (SP2) {
;             PG8_LDB(B0, 0, 0); PG8_LDB(B1, 0, 1); PG8_SCHED; PG8_LDA(At, 0, 0); PG8_STAGE(PG8_SA(1, 1), a1 + hstep, voffA);
;             PG8_WAIT_V(8); PG8_WAIT_L(0); PG8_BAR; PG8_MMA(0, 0, At, B0); PG8_MMA(0, 1, At, B1); PG8_BAR; PG8_SCHED;
;             PG8_LDA(At, 0, 1); PG8_STAGE(PG8_SB(0, 0), b2, voffB); PG8_STAGE(PG8_SB(0, 1), b2 + hstep, voffB); PG8_STAGE(PG8_SA(0, 0), a2, voffA);
;             PG8_WAIT_V(8); PG8_WAIT_L(0); PG8_BAR; PG8_MMA(1, 0, At, B0); PG8_MMA(1, 1, At, B1); PG8_BAR; PG8_SCHED;
.LBB0_563:
	ds_read_b128 v[146:149], v154
	ds_read_b128 v[158:161], v154 offset:1024
	ds_read_b128 v[162:165], v154 offset:2048
	ds_read_b128 v[166:169], v154 offset:3072
	ds_read_b128 v[170:173], v155
	ds_read_b128 v[174:177], v155 offset:1024
	ds_read_b128 v[178:181], v155 offset:2048
	ds_read_b128 v[184:187], v155 offset:3072
	s_add_u32 s30, s28, 0xffe00080
	s_addc_u32 s31, s29, -1
	s_cmpk_eq_i32 s51, 0x7c
	s_cselect_b32 s35, s21, s31
	s_cselect_b32 s34, s47, s30
	s_cselect_b32 s31, s19, s50
	s_cselect_b32 s30, s48, s49
	s_nop 0
	s_add_i32 m0, s27, 0xc000
	ds_read_b128 v[188:191], v156
	ds_read_b128 v[192:195], v156 offset:1024
	ds_read_b128 v[196:199], v156 offset:2048
	ds_read_b128 v[200:203], v156 offset:3072
	ds_read_b128 v[204:207], v156 offset:4096
	ds_read_b128 v[208:211], v156 offset:5120
	ds_read_b128 v[212:215], v156 offset:6144
	ds_read_b128 v[216:219], v156 offset:7168
	global_load_lds_dwordx4 v138, s[28:29]
	s_nop 0
	s_add_i32 m0, s27, 0xe000
	s_nop 0
	global_load_lds_dwordx4 v140, s[28:29]
	s_waitcnt vmcnt(8)
	s_waitcnt lgkmcnt(0)
	s_barrier
	s_setprio 1
	s_waitcnt lgkmcnt(0)
	v_mfma_f32_16x16x32_bf16 v[126:129], v[146:149], v[188:191], v[126:129]
	v_mfma_f32_16x16x32_bf16 v[122:125], v[162:165], v[188:191], v[122:125]
	v_mfma_f32_16x16x32_bf16 v[110:113], v[146:149], v[196:199], v[110:113]
	v_mfma_f32_16x16x32_bf16 v[106:109], v[162:165], v[196:199], v[106:109]
	v_mfma_f32_16x16x32_bf16 v[94:97], v[146:149], v[204:207], v[94:97]
	v_mfma_f32_16x16x32_bf16 v[90:93], v[162:165], v[204:207], v[90:93]
	v_mfma_f32_16x16x32_bf16 v[78:81], v[146:149], v[212:215], v[78:81]
	v_mfma_f32_16x16x32_bf16 v[74:77], v[162:165], v[212:215], v[74:77]
	v_mfma_f32_16x16x32_bf16 v[126:129], v[158:161], v[192:195], v[126:129]
	v_mfma_f32_16x16x32_bf16 v[122:125], v[166:169], v[192:195], v[122:125]
	v_mfma_f32_16x16x32_bf16 v[110:113], v[158:161], v[200:203], v[110:113]
	v_mfma_f32_16x16x32_bf16 v[106:109], v[166:169], v[200:203], v[106:109]
	v_mfma_f32_16x16x32_bf16 v[94:97], v[158:161], v[208:211], v[94:97]
	v_mfma_f32_16x16x32_bf16 v[90:93], v[166:169], v[208:211], v[90:93]
	v_mfma_f32_16x16x32_bf16 v[78:81], v[158:161], v[216:219], v[78:81]
	v_mfma_f32_16x16x32_bf16 v[74:77], v[166:169], v[216:219], v[74:77]
	s_setprio 0
	s_setprio 1
	v_mfma_f32_16x16x32_bf16 v[118:121], v[170:173], v[188:191], v[118:121]
	v_mfma_f32_16x16x32_bf16 v[114:117], v[178:181], v[188:191], v[114:117]
	v_mfma_f32_16x16x32_bf16 v[102:105], v[170:173], v[196:199], v[102:105]
	v_mfma_f32_16x16x32_bf16 v[98:101], v[178:181], v[196:199], v[98:101]
	v_mfma_f32_16x16x32_bf16 v[86:89], v[170:173], v[204:207], v[86:89]
	v_mfma_f32_16x16x32_bf16 v[82:85], v[178:181], v[204:207], v[82:85]
	v_mfma_f32_16x16x32_bf16 v[70:73], v[170:173], v[212:215], v[70:73]
	v_mfma_f32_16x16x32_bf16 v[66:69], v[178:181], v[212:215], v[66:69]
	v_mfma_f32_16x16x32_bf16 v[118:121], v[174:177], v[192:195], v[118:121]
	v_mfma_f32_16x16x32_bf16 v[114:117], v[184:187], v[192:195], v[114:117]
	v_mfma_f32_16x16x32_bf16 v[102:105], v[174:177], v[200:203], v[102:105]
	v_mfma_f32_16x16x32_bf16 v[98:101], v[184:187], v[200:203], v[98:101]
	v_mfma_f32_16x16x32_bf16 v[86:89], v[174:177], v[208:211], v[86:89]
	v_mfma_f32_16x16x32_bf16 v[82:85], v[184:187], v[208:211], v[82:85]
	v_mfma_f32_16x16x32_bf16 v[70:73], v[174:177], v[216:219], v[70:73]
	v_mfma_f32_16x16x32_bf16 v[66:69], v[184:187], v[216:219], v[66:69]
	s_setprio 0
	s_barrier
	s_add_i32 s52, s44, s36
	s_nop 0
	s_mov_b32 m0, s52
	ds_read_b128 v[188:191], v156 offset:16384
	ds_read_b128 v[192:195], v156 offset:17408
	ds_read_b128 v[196:199], v156 offset:18432
	ds_read_b128 v[200:203], v156 offset:19456
	ds_read_b128 v[204:207], v156 offset:20480
	ds_read_b128 v[208:211], v156 offset:21504
	ds_read_b128 v[212:215], v156 offset:22528
	ds_read_b128 v[216:219], v156 offset:23552
	global_load_lds_dwordx4 v132, s[30:31]
	s_add_i32 m0, s52, 0x2000
	s_add_u32 s52, s30, 0x200000
	s_nop 0
	s_addc_u32 s53, s31, 0
	s_add_i32 s54, s45, s36
	global_load_lds_dwordx4 v136, s[30:31]
	s_nop 0
	s_mov_b32 m0, s54
	s_add_u32 s60, s34, s2
	s_addc_u32 s61, s35, s3
	global_load_lds_dwordx4 v132, s[52:53]
	s_nop 0
	s_add_i32 m0, s54, 0x2000
	s_nop 0
	global_load_lds_dwordx4 v136, s[52:53]
	s_nop 0
	s_mov_b32 m0, s27
	s_nop 0
	global_load_lds_dwordx4 v130, s[34:35]
	s_mov_b32 m0, s37
	s_nop 0
	global_load_lds_dwordx4 v134, s[34:35]
	s_waitcnt vmcnt(8)
	s_waitcnt lgkmcnt(0)
	s_barrier
	s_setprio 1
	s_waitcnt lgkmcnt(0)
	v_mfma_f32_16x16x32_bf16 v[62:65], v[146:149], v[188:191], v[62:65]
	v_mfma_f32_16x16x32_bf16 v[58:61], v[162:165], v[188:191], v[58:61]
	v_mfma_f32_16x16x32_bf16 v[46:49], v[146:149], v[196:199], v[46:49]
	v_mfma_f32_16x16x32_bf16 v[42:45], v[162:165], v[196:199], v[42:45]
	v_mfma_f32_16x16x32_bf16 v[30:33], v[146:149], v[204:207], v[30:33]
	v_mfma_f32_16x16x32_bf16 v[26:29], v[162:165], v[204:207], v[26:29]
	v_mfma_f32_16x16x32_bf16 v[14:17], v[146:149], v[212:215], v[14:17]
	v_mfma_f32_16x16x32_bf16 v[10:13], v[162:165], v[212:215], v[10:13]
	v_mfma_f32_16x16x32_bf16 v[62:65], v[158:161], v[192:195], v[62:65]
	v_mfma_f32_16x16x32_bf16 v[58:61], v[166:169], v[192:195], v[58:61]
	v_mfma_f32_16x16x32_bf16 v[46:49], v[158:161], v[200:203], v[46:49]
	v_mfma_f32_16x16x32_bf16 v[42:45], v[166:169], v[200:203], v[42:45]
	v_mfma_f32_16x16x32_bf16 v[30:33], v[158:161], v[208:211], v[30:33]
	v_mfma_f32_16x16x32_bf16 v[26:29], v[166:169], v[208:211], v[26:29]
	v_mfma_f32_16x16x32_bf16 v[14:17], v[158:161], v[216:219], v[14:17]
	v_mfma_f32_16x16x32_bf16 v[10:13], v[166:169], v[216:219], v[10:13]
	s_setprio 0
	s_setprio 1
	v_mfma_f32_16x16x32_bf16 v[54:57], v[170:173], v[188:191], v[54:57]
	v_mfma_f32_16x16x32_bf16 v[50:53], v[178:181], v[188:191], v[50:53]
	v_mfma_f32_16x16x32_bf16 v[38:41], v[170:173], v[196:199], v[38:41]
	v_mfma_f32_16x16x32_bf16 v[34:37], v[178:181], v[196:199], v[34:37]
	v_mfma_f32_16x16x32_bf16 v[22:25], v[170:173], v[204:207], v[22:25]
	v_mfma_f32_16x16x32_bf16 v[18:21], v[178:181], v[204:207], v[18:21]
	v_mfma_f32_16x16x32_bf16 v[6:9], v[170:173], v[212:215], v[6:9]
	v_mfma_f32_16x16x32_bf16 v[2:5], v[178:181], v[212:215], v[2:5]
	v_mfma_f32_16x16x32_bf16 v[54:57], v[174:177], v[192:195], v[54:57]
	v_mfma_f32_16x16x32_bf16 v[50:53], v[184:187], v[192:195], v[50:53]
	v_mfma_f32_16x16x32_bf16 v[38:41], v[174:177], v[200:203], v[38:41]
	v_mfma_f32_16x16x32_bf16 v[34:37], v[184:187], v[200:203], v[34:37]
	v_mfma_f32_16x16x32_bf16 v[22:25], v[174:177], v[208:211], v[22:25]
	v_mfma_f32_16x16x32_bf16 v[18:21], v[184:187], v[208:211], v[18:21]
	v_mfma_f32_16x16x32_bf16 v[6:9], v[174:177], v[216:219], v[6:9]
	v_mfma_f32_16x16x32_bf16 v[2:5], v[184:187], v[216:219], v[2:5]
	s_setprio 0
	s_barrier
; #define PG8_STAGE(bufoff, gbase, voff) do { _Pragma("unroll") for (int _i = 0; _i < 2; ++_i) \
;         __builtin_amdgcn_global_load_lds((const unsigned*)((const char*)(gbase) + (voff)[_i]), (PG8_LAS unsigned*)(lds + (bufoff) + ldsw + _i * 8192), 16, 0, 0); } while (0)
; #define PG8_LDA(dst, b, h) do { _Pragma("unroll") for (int m = 0; m < 4; ++m) _Pragma("unroll") for (int k = 0; k < 2; ++k) dst[m][k] = *(const PG8_LAS bf16x8*)(lds + PG8_SA(b, h) + aoff + m * 2048 + k * 1024); } while (0)
; #define PG8_LDB(dst, b, h) do { _Pragma("unroll") for (int n = 0; n < 2; ++n) _Pragma("unroll") for (int k = 0; k < 2; ++k) dst[n][k] = *(const PG8_LAS bf16x8*)(lds + PG8_SB(b, h) + boff + n * 2048 + k * 1024); } while (0)
; #define PG8_MMA(ai, bj, At, Bt) do { __builtin_amdgcn_s_setprio(1); _Pragma("unroll") for (int m = 0; m < 4; ++m) _Pragma("unroll") for (int n = 0; n < 2; ++n) _Pragma("unroll") for (int k = 0; k < 2; ++k) \
;         acc[ai][bj][m][n] = __builtin_amdgcn_mfma_f32_16x16x32_bf16(Bt[n][k], At[m][k], acc[ai][bj][m][n], 0, 0, 0); __builtin_amdgcn_s_setprio(0); } while (0)
; #define PG8_WAIT_V(n) asm volatile("s_waitcnt vmcnt(" #n ")" ::: "memory")
; #define PG8_WAIT_L(n) asm volatile("s_waitcnt lgkmcnt(" #n ")" ::: "memory")
; #define PG8_BAR __builtin_amdgcn_s_barrier()
; #define PG8_SCHED __builtin_amdgcn_sched_barrier(0)
; template <class Epi, class Sched, bool ALIGN_EPI = false, bool SP2 = false>
; __device__ __forceinline__ void gemm_phase(PG8_LAS unsigned char* lds, const Gemm g, const Sched& S, const Epi& E) {
;     ...
;             PG8_LDB(B0, 1, 0); PG8_LDB(B1, 1, 1); PG8_SCHED; PG8_LDA(At, 1, 0); PG8_STAGE(PG8_SA(0, 1), a2 + hstep, voffA);
;             PG8_WAIT_V(8); PG8_WAIT_L(0); PG8_BAR; PG8_MMA(0, 0, At, B0); PG8_MMA(0, 1, At, B1); PG8_BAR; PG8_SCHED;
;             PG8_LDA(At, 1, 1); PG8_STAGE(PG8_SB(1, 0), b3, voffB); PG8_STAGE(PG8_SB(1, 1), b3 + hstep, voffB); PG8_STAGE(PG8_SA(1, 0), a3, voffA);
;             PG8_WAIT_V(8); PG8_WAIT_L(0); PG8_BAR; PG8_MMA(1, 0, At, B0); PG8_MMA(1, 1, At, B1); PG8_BAR; PG8_SCHED;
;     ...
;         if constexpr (ALIGN_EPI) { if (wr == 0) PG8_BAR; }
	s_add_i32 s52, 0, 0x18000
	v_add_u32_e32 v157, s52, v152
	s_add_i32 s53, 0, 0x1c000
	ds_read_b128 v[146:149], v157
	ds_read_b128 v[158:161], v157 offset:1024
	ds_read_b128 v[162:165], v157 offset:2048
	ds_read_b128 v[166:169], v157 offset:3072
	v_add_u32_e32 v157, s53, v152
	ds_read_b128 v[170:173], v157
	ds_read_b128 v[174:177], v157 offset:1024
	ds_read_b128 v[178:181], v157 offset:2048
	ds_read_b128 v[184:187], v157 offset:3072
	s_add_u32 s34, s34, 0x200000
	s_addc_u32 s35, s35, 0
	s_mov_b32 m0, s38
	s_nop 0
	ds_read_b128 v[188:191], v156 offset:32768
	ds_read_b128 v[192:195], v156 offset:33792
	ds_read_b128 v[196:199], v156 offset:34816
	ds_read_b128 v[200:203], v156 offset:35840
	ds_read_b128 v[204:207], v156 offset:36864
	ds_read_b128 v[208:211], v156 offset:37888
	ds_read_b128 v[212:215], v156 offset:38912
	ds_read_b128 v[216:219], v156 offset:39936
	global_load_lds_dwordx4 v130, s[34:35]
	s_nop 0
	s_mov_b32 m0, s39
	s_nop 0
	global_load_lds_dwordx4 v134, s[34:35]
	s_waitcnt vmcnt(8)
	s_waitcnt lgkmcnt(0)
	s_barrier
	s_setprio 1
	s_waitcnt lgkmcnt(0)
	v_mfma_f32_16x16x32_bf16 v[126:129], v[146:149], v[188:191], v[126:129]
	v_mfma_f32_16x16x32_bf16 v[122:125], v[162:165], v[188:191], v[122:125]
	v_mfma_f32_16x16x32_bf16 v[110:113], v[146:149], v[196:199], v[110:113]
	v_mfma_f32_16x16x32_bf16 v[106:109], v[162:165], v[196:199], v[106:109]
	v_mfma_f32_16x16x32_bf16 v[94:97], v[146:149], v[204:207], v[94:97]
	v_mfma_f32_16x16x32_bf16 v[90:93], v[162:165], v[204:207], v[90:93]
	v_mfma_f32_16x16x32_bf16 v[78:81], v[146:149], v[212:215], v[78:81]
	v_mfma_f32_16x16x32_bf16 v[74:77], v[162:165], v[212:215], v[74:77]
	v_mfma_f32_16x16x32_bf16 v[126:129], v[158:161], v[192:195], v[126:129]
	v_mfma_f32_16x16x32_bf16 v[122:125], v[166:169], v[192:195], v[122:125]
	v_mfma_f32_16x16x32_bf16 v[110:113], v[158:161], v[200:203], v[110:113]
	v_mfma_f32_16x16x32_bf16 v[106:109], v[166:169], v[200:203], v[106:109]
	v_mfma_f32_16x16x32_bf16 v[94:97], v[158:161], v[208:211], v[94:97]
	v_mfma_f32_16x16x32_bf16 v[90:93], v[166:169], v[208:211], v[90:93]
	v_mfma_f32_16x16x32_bf16 v[78:81], v[158:161], v[216:219], v[78:81]
	v_mfma_f32_16x16x32_bf16 v[74:77], v[166:169], v[216:219], v[74:77]
	s_setprio 0
	s_setprio 1
	v_mfma_f32_16x16x32_bf16 v[118:121], v[170:173], v[188:191], v[118:121]
	v_mfma_f32_16x16x32_bf16 v[114:117], v[178:181], v[188:191], v[114:117]
	v_mfma_f32_16x16x32_bf16 v[102:105], v[170:173], v[196:199], v[102:105]
	v_mfma_f32_16x16x32_bf16 v[98:101], v[178:181], v[196:199], v[98:101]
	v_mfma_f32_16x16x32_bf16 v[86:89], v[170:173], v[204:207], v[86:89]
	v_mfma_f32_16x16x32_bf16 v[82:85], v[178:181], v[204:207], v[82:85]
	v_mfma_f32_16x16x32_bf16 v[70:73], v[170:173], v[212:215], v[70:73]
	v_mfma_f32_16x16x32_bf16 v[66:69], v[178:181], v[212:215], v[66:69]
	v_mfma_f32_16x16x32_bf16 v[118:121], v[174:177], v[192:195], v[118:121]
	v_mfma_f32_16x16x32_bf16 v[114:117], v[184:187], v[192:195], v[114:117]
	v_mfma_f32_16x16x32_bf16 v[102:105], v[174:177], v[200:203], v[102:105]
	v_mfma_f32_16x16x32_bf16 v[98:101], v[184:187], v[200:203], v[98:101]
	v_mfma_f32_16x16x32_bf16 v[86:89], v[174:177], v[208:211], v[86:89]
	v_mfma_f32_16x16x32_bf16 v[82:85], v[184:187], v[208:211], v[82:85]
	v_mfma_f32_16x16x32_bf16 v[70:73], v[174:177], v[216:219], v[70:73]
	v_mfma_f32_16x16x32_bf16 v[66:69], v[184:187], v[216:219], v[66:69]
	s_setprio 0
	s_barrier
	s_add_i32 s34, s52, s36
	s_add_u32 s58, s30, s2
	s_addc_u32 s59, s31, s3
	s_mov_b32 m0, s34
	ds_read_b128 v[188:191], v156 offset:49152
	ds_read_b128 v[192:195], v156 offset:50176
	ds_read_b128 v[196:199], v156 offset:51200
	ds_read_b128 v[200:203], v156 offset:52224
	ds_read_b128 v[204:207], v156 offset:53248
	ds_read_b128 v[208:211], v156 offset:54272
	ds_read_b128 v[212:215], v156 offset:55296
	ds_read_b128 v[216:219], v156 offset:56320
	global_load_lds_dwordx4 v132, s[58:59]
	s_add_i32 m0, s34, 0x2000
	s_add_u32 s30, s30, 0x200080
	s_nop 0
	s_addc_u32 s31, s31, 0
	s_add_i32 s34, s53, s36
	global_load_lds_dwordx4 v136, s[58:59]
	s_nop 0
	s_mov_b32 m0, s34
	s_nop 0
	global_load_lds_dwordx4 v132, s[30:31]
	s_nop 0
	s_add_i32 m0, s34, 0x2000
	s_nop 0
	global_load_lds_dwordx4 v136, s[30:31]
	s_nop 0
	s_mov_b32 m0, s41
	s_nop 0
	global_load_lds_dwordx4 v130, s[60:61]
	s_nop 0
	s_mov_b32 m0, s42
	s_nop 0
	global_load_lds_dwordx4 v134, s[60:61]
	s_waitcnt vmcnt(8)
	s_waitcnt lgkmcnt(0)
	s_barrier
	s_setprio 1
	s_waitcnt lgkmcnt(0)
	v_mfma_f32_16x16x32_bf16 v[62:65], v[146:149], v[188:191], v[62:65]
	v_mfma_f32_16x16x32_bf16 v[58:61], v[162:165], v[188:191], v[58:61]
	v_mfma_f32_16x16x32_bf16 v[46:49], v[146:149], v[196:199], v[46:49]
	v_mfma_f32_16x16x32_bf16 v[42:45], v[162:165], v[196:199], v[42:45]
	v_mfma_f32_16x16x32_bf16 v[30:33], v[146:149], v[204:207], v[30:33]
	v_mfma_f32_16x16x32_bf16 v[26:29], v[162:165], v[204:207], v[26:29]
	v_mfma_f32_16x16x32_bf16 v[14:17], v[146:149], v[212:215], v[14:17]
	v_mfma_f32_16x16x32_bf16 v[10:13], v[162:165], v[212:215], v[10:13]
	v_mfma_f32_16x16x32_bf16 v[62:65], v[158:161], v[192:195], v[62:65]
	v_mfma_f32_16x16x32_bf16 v[58:61], v[166:169], v[192:195], v[58:61]
	v_mfma_f32_16x16x32_bf16 v[46:49], v[158:161], v[200:203], v[46:49]
	v_mfma_f32_16x16x32_bf16 v[42:45], v[166:169], v[200:203], v[42:45]
	v_mfma_f32_16x16x32_bf16 v[30:33], v[158:161], v[208:211], v[30:33]
	v_mfma_f32_16x16x32_bf16 v[26:29], v[166:169], v[208:211], v[26:29]
	v_mfma_f32_16x16x32_bf16 v[14:17], v[158:161], v[216:219], v[14:17]
	v_mfma_f32_16x16x32_bf16 v[10:13], v[166:169], v[216:219], v[10:13]
	s_setprio 0
	s_setprio 1
	v_mfma_f32_16x16x32_bf16 v[54:57], v[170:173], v[188:191], v[54:57]
	v_mfma_f32_16x16x32_bf16 v[50:53], v[178:181], v[188:191], v[50:53]
	v_mfma_f32_16x16x32_bf16 v[38:41], v[170:173], v[196:199], v[38:41]
	v_mfma_f32_16x16x32_bf16 v[34:37], v[178:181], v[196:199], v[34:37]
	v_mfma_f32_16x16x32_bf16 v[22:25], v[170:173], v[204:207], v[22:25]
	v_mfma_f32_16x16x32_bf16 v[18:21], v[178:181], v[204:207], v[18:21]
	v_mfma_f32_16x16x32_bf16 v[6:9], v[170:173], v[212:215], v[6:9]
	v_mfma_f32_16x16x32_bf16 v[2:5], v[178:181], v[212:215], v[2:5]
	v_mfma_f32_16x16x32_bf16 v[54:57], v[174:177], v[192:195], v[54:57]
	v_mfma_f32_16x16x32_bf16 v[50:53], v[184:187], v[192:195], v[50:53]
	v_mfma_f32_16x16x32_bf16 v[38:41], v[174:177], v[200:203], v[38:41]
	v_mfma_f32_16x16x32_bf16 v[34:37], v[184:187], v[200:203], v[34:37]
	v_mfma_f32_16x16x32_bf16 v[22:25], v[174:177], v[208:211], v[22:25]
	v_mfma_f32_16x16x32_bf16 v[18:21], v[184:187], v[208:211], v[18:21]
	v_mfma_f32_16x16x32_bf16 v[6:9], v[174:177], v[216:219], v[6:9]
	v_mfma_f32_16x16x32_bf16 v[2:5], v[184:187], v[216:219], v[2:5]
	s_setprio 0
	s_barrier
	s_add_i32 s51, s51, 2
	s_add_u32 s28, s28, 0x100
	s_addc_u32 s29, s29, 0
	s_add_u32 s49, s49, 0x100
	s_addc_u32 s50, s50, 0
	s_cmpk_gt_u32 s51, 0x7d
	s_cbranch_scc0 .LBB0_563
	s_and_b64 vcc, exec, s[8:9]
	s_cbranch_vccz .LBB0_566
	s_barrier

; #define PG8_STAGE(bufoff, gbase, voff) do { _Pragma("unroll") for (int _i = 0; _i < 2; ++_i) \
;         __builtin_amdgcn_global_load_lds((const unsigned*)((const char*)(gbase) + (voff)[_i]), (PG8_LAS unsigned*)(lds + (bufoff) + ldsw + _i * 8192), 16, 0, 0); } while (0)
; #define PG8_LDA(dst, b, h) do { _Pragma("unroll") for (int m = 0; m < 4; ++m) _Pragma("unroll") for (int k = 0; k < 2; ++k) dst[m][k] = *(const PG8_LAS bf16x8*)(lds + PG8_SA(b, h) + aoff + m * 2048 + k * 1024); } while (0)
; #define PG8_LDB(dst, b, h) do { _Pragma("unroll") for (int n = 0; n < 2; ++n) _Pragma("unroll") for (int k = 0; k < 2; ++k) dst[n][k] = *(const PG8_LAS bf16x8*)(lds + PG8_SB(b, h) + boff + n * 2048 + k * 1024); } while (0)
; #define PG8_MMA(ai, bj, At, Bt) do { __builtin_amdgcn_s_setprio(1); _Pragma("unroll") for (int m = 0; m < 4; ++m) _Pragma("unroll") for (int n = 0; n < 2; ++n) _Pragma("unroll") for (int k = 0; k < 2; ++k) \
;         acc[ai][bj][m][n] = __builtin_amdgcn_mfma_f32_16x16x32_bf16(Bt[n][k], At[m][k], acc[ai][bj][m][n], 0, 0, 0); __builtin_amdgcn_s_setprio(0); } while (0)
; #define PG8_WAIT_V(n) asm volatile("s_waitcnt vmcnt(" #n ")" ::: "memory")
; #define PG8_WAIT_L(n) asm volatile("s_waitcnt lgkmcnt(" #n ")" ::: "memory")
; template <class Epi, class Sched, bool ALIGN_EPI = false, bool SP2 = false>
; __device__ __forceinline__ void gemm_phase(PG8_LAS unsigned char* lds, const Gemm g, const Sched& S, const Epi& E) {
;     ...
;             const bool last = (t == nt - 2);
;             const char* a1 = cA + (size_t)(t + 1) * kstep;
;             const char* a2 = last ? nA : cA + (size_t)(t + 2) * kstep; const char* b2 = last ? nB : cB + (size_t)(t + 2) * kstep;
;             const char* a3 = a2 + kstep; const char* b3 = b2 + kstep;
;             if (last && has_next) S.a_ready(nxt);
;             if constexpr (SP2) {
;             PG8_LDB(B0, 0, 0); PG8_LDB(B1, 0, 1); PG8_SCHED; PG8_LDA(At, 0, 0); PG8_STAGE(PG8_SA(1, 1), a1 + hstep, voffA);
;             PG8_WAIT_V(8); PG8_WAIT_L(0); PG8_BAR; PG8_MMA(0, 0, At, B0); PG8_MMA(0, 1, At, B1); PG8_BAR; PG8_SCHED;
;             PG8_LDA(At, 0, 1); PG8_STAGE(PG8_SB(0, 0), b2, voffB); PG8_STAGE(PG8_SB(0, 1), b2 + hstep, voffB); PG8_STAGE(PG8_SA(0, 0), a2, voffA);
;             PG8_WAIT_V(8); PG8_WAIT_L(0); PG8_BAR; PG8_MMA(1, 0, At, B0); PG8_MMA(1, 1, At, B1); PG8_BAR; PG8_SCHED;
.LBB0_707:
	ds_read_b128 v[142:145], v151
	ds_read_b128 v[154:157], v151 offset:1024
	ds_read_b128 v[158:161], v151 offset:2048
	ds_read_b128 v[162:165], v151 offset:3072
	ds_read_b128 v[166:169], v152
	ds_read_b128 v[170:173], v152 offset:1024
	ds_read_b128 v[174:177], v152 offset:2048
	ds_read_b128 v[178:181], v152 offset:3072
	s_add_u32 s34, s30, 0xfff00080
	s_addc_u32 s35, s31, -1
	s_cmp_eq_u32 s61, 60
	s_cselect_b32 s37, s25, s35
	s_cselect_b32 s36, s57, s34
	s_cselect_b32 s35, s23, s60
	s_cselect_b32 s34, s58, s59
	s_nop 0
	s_add_i32 m0, s42, 0xc000
	ds_read_b128 v[184:187], v153
	ds_read_b128 v[188:191], v153 offset:1024
	ds_read_b128 v[192:195], v153 offset:2048
	ds_read_b128 v[196:199], v153 offset:3072
	ds_read_b128 v[200:203], v153 offset:4096
	ds_read_b128 v[204:207], v153 offset:5120
	ds_read_b128 v[208:211], v153 offset:6144
	ds_read_b128 v[212:215], v153 offset:7168
	global_load_lds_dwordx4 v134, s[30:31]
	s_nop 0
	s_add_i32 m0, s42, 0xe000
	s_nop 0
	global_load_lds_dwordx4 v136, s[30:31]
	s_waitcnt vmcnt(8)
	s_waitcnt lgkmcnt(0)
	s_barrier
	s_setprio 1
	s_waitcnt lgkmcnt(0)
	v_mfma_f32_16x16x32_bf16 v[126:129], v[142:145], v[184:187], v[126:129]
	v_mfma_f32_16x16x32_bf16 v[122:125], v[158:161], v[184:187], v[122:125]
	v_mfma_f32_16x16x32_bf16 v[110:113], v[142:145], v[192:195], v[110:113]
	v_mfma_f32_16x16x32_bf16 v[106:109], v[158:161], v[192:195], v[106:109]
	v_mfma_f32_16x16x32_bf16 v[94:97], v[142:145], v[200:203], v[94:97]
	v_mfma_f32_16x16x32_bf16 v[90:93], v[158:161], v[200:203], v[90:93]
	v_mfma_f32_16x16x32_bf16 v[86:89], v[142:145], v[208:211], v[86:89]
	v_mfma_f32_16x16x32_bf16 v[78:81], v[158:161], v[208:211], v[78:81]
	v_mfma_f32_16x16x32_bf16 v[126:129], v[154:157], v[188:191], v[126:129]
	v_mfma_f32_16x16x32_bf16 v[122:125], v[162:165], v[188:191], v[122:125]
	v_mfma_f32_16x16x32_bf16 v[110:113], v[154:157], v[196:199], v[110:113]
	v_mfma_f32_16x16x32_bf16 v[106:109], v[162:165], v[196:199], v[106:109]
	v_mfma_f32_16x16x32_bf16 v[94:97], v[154:157], v[204:207], v[94:97]
	v_mfma_f32_16x16x32_bf16 v[90:93], v[162:165], v[204:207], v[90:93]
	v_mfma_f32_16x16x32_bf16 v[86:89], v[154:157], v[212:215], v[86:89]
	v_mfma_f32_16x16x32_bf16 v[78:81], v[162:165], v[212:215], v[78:81]
	s_setprio 0
	s_setprio 1
	v_mfma_f32_16x16x32_bf16 v[118:121], v[166:169], v[184:187], v[118:121]
	v_mfma_f32_16x16x32_bf16 v[114:117], v[174:177], v[184:187], v[114:117]
	v_mfma_f32_16x16x32_bf16 v[102:105], v[166:169], v[192:195], v[102:105]
	v_mfma_f32_16x16x32_bf16 v[98:101], v[174:177], v[192:195], v[98:101]
	v_mfma_f32_16x16x32_bf16 v[82:85], v[166:169], v[200:203], v[82:85]
	v_mfma_f32_16x16x32_bf16 v[74:77], v[174:177], v[200:203], v[74:77]
	v_mfma_f32_16x16x32_bf16 v[70:73], v[166:169], v[208:211], v[70:73]
	v_mfma_f32_16x16x32_bf16 v[66:69], v[174:177], v[208:211], v[66:69]
	v_mfma_f32_16x16x32_bf16 v[118:121], v[170:173], v[188:191], v[118:121]
	v_mfma_f32_16x16x32_bf16 v[114:117], v[178:181], v[188:191], v[114:117]
	v_mfma_f32_16x16x32_bf16 v[102:105], v[170:173], v[196:199], v[102:105]
	v_mfma_f32_16x16x32_bf16 v[98:101], v[178:181], v[196:199], v[98:101]
	v_mfma_f32_16x16x32_bf16 v[82:85], v[170:173], v[204:207], v[82:85]
	v_mfma_f32_16x16x32_bf16 v[74:77], v[178:181], v[204:207], v[74:77]
	v_mfma_f32_16x16x32_bf16 v[70:73], v[170:173], v[212:215], v[70:73]
	v_mfma_f32_16x16x32_bf16 v[66:69], v[178:181], v[212:215], v[66:69]
	s_setprio 0
	s_barrier
	s_add_i32 s62, s51, s33
	s_nop 0
	s_mov_b32 m0, s62
	ds_read_b128 v[184:187], v153 offset:16384
	ds_read_b128 v[188:191], v153 offset:17408
	ds_read_b128 v[192:195], v153 offset:18432
	ds_read_b128 v[196:199], v153 offset:19456
	ds_read_b128 v[200:203], v153 offset:20480
	ds_read_b128 v[204:207], v153 offset:21504
	ds_read_b128 v[208:211], v153 offset:22528
	ds_read_b128 v[212:215], v153 offset:23552
	global_load_lds_dwordx4 v130, s[34:35]
	s_add_i32 m0, s62, 0x2000
	s_add_u32 s62, s34, 0x100000
	s_nop 0
	s_addc_u32 s63, s35, 0
	s_add_i32 s72, s52, s33
	global_load_lds_dwordx4 v132, s[34:35]
	s_nop 0
	s_mov_b32 m0, s72
	s_add_u32 s84, s36, s12
	s_addc_u32 s85, s37, s13
	global_load_lds_dwordx4 v130, s[62:63]
	s_nop 0
	s_add_i32 m0, s72, 0x2000
	s_nop 0
	global_load_lds_dwordx4 v132, s[62:63]
	s_nop 0
	s_mov_b32 m0, s42
	s_nop 0
	global_load_lds_dwordx4 v130, s[36:37]
	s_mov_b32 m0, s43
	s_nop 0
	global_load_lds_dwordx4 v132, s[36:37]
	s_waitcnt vmcnt(8)
	s_waitcnt lgkmcnt(0)
	s_barrier
	s_setprio 1
	s_waitcnt lgkmcnt(0)
	v_mfma_f32_16x16x32_bf16 v[62:65], v[142:145], v[184:187], v[62:65]
	v_mfma_f32_16x16x32_bf16 v[58:61], v[158:161], v[184:187], v[58:61]
	v_mfma_f32_16x16x32_bf16 v[50:53], v[142:145], v[192:195], v[50:53]
	v_mfma_f32_16x16x32_bf16 v[42:45], v[158:161], v[192:195], v[42:45]
	v_mfma_f32_16x16x32_bf16 v[34:37], v[142:145], v[200:203], v[34:37]
	v_mfma_f32_16x16x32_bf16 v[26:29], v[158:161], v[200:203], v[26:29]
	v_mfma_f32_16x16x32_bf16 v[14:17], v[142:145], v[208:211], v[14:17]
	v_mfma_f32_16x16x32_bf16 v[10:13], v[158:161], v[208:211], v[10:13]
	v_mfma_f32_16x16x32_bf16 v[62:65], v[154:157], v[188:191], v[62:65]
	v_mfma_f32_16x16x32_bf16 v[58:61], v[162:165], v[188:191], v[58:61]
	v_mfma_f32_16x16x32_bf16 v[50:53], v[154:157], v[196:199], v[50:53]
	v_mfma_f32_16x16x32_bf16 v[42:45], v[162:165], v[196:199], v[42:45]
	v_mfma_f32_16x16x32_bf16 v[34:37], v[154:157], v[204:207], v[34:37]
	v_mfma_f32_16x16x32_bf16 v[26:29], v[162:165], v[204:207], v[26:29]
	v_mfma_f32_16x16x32_bf16 v[14:17], v[154:157], v[212:215], v[14:17]
	v_mfma_f32_16x16x32_bf16 v[10:13], v[162:165], v[212:215], v[10:13]
	s_setprio 0
	s_setprio 1
	v_mfma_f32_16x16x32_bf16 v[54:57], v[166:169], v[184:187], v[54:57]
	v_mfma_f32_16x16x32_bf16 v[46:49], v[174:177], v[184:187], v[46:49]
	v_mfma_f32_16x16x32_bf16 v[38:41], v[166:169], v[192:195], v[38:41]
	v_mfma_f32_16x16x32_bf16 v[30:33], v[174:177], v[192:195], v[30:33]
	v_mfma_f32_16x16x32_bf16 v[22:25], v[166:169], v[200:203], v[22:25]
	v_mfma_f32_16x16x32_bf16 v[18:21], v[174:177], v[200:203], v[18:21]
	v_mfma_f32_16x16x32_bf16 v[6:9], v[166:169], v[208:211], v[6:9]
	v_mfma_f32_16x16x32_bf16 v[2:5], v[174:177], v[208:211], v[2:5]
	v_mfma_f32_16x16x32_bf16 v[54:57], v[170:173], v[188:191], v[54:57]
	v_mfma_f32_16x16x32_bf16 v[46:49], v[178:181], v[188:191], v[46:49]
	v_mfma_f32_16x16x32_bf16 v[38:41], v[170:173], v[196:199], v[38:41]
	v_mfma_f32_16x16x32_bf16 v[30:33], v[178:181], v[196:199], v[30:33]
	v_mfma_f32_16x16x32_bf16 v[22:25], v[170:173], v[204:207], v[22:25]
	v_mfma_f32_16x16x32_bf16 v[18:21], v[178:181], v[204:207], v[18:21]
	v_mfma_f32_16x16x32_bf16 v[6:9], v[170:173], v[212:215], v[6:9]
	v_mfma_f32_16x16x32_bf16 v[2:5], v[178:181], v[212:215], v[2:5]
	s_setprio 0
	s_barrier
; #define PG8_STAGE(bufoff, gbase, voff) do { _Pragma("unroll") for (int _i = 0; _i < 2; ++_i) \
;         __builtin_amdgcn_global_load_lds((const unsigned*)((const char*)(gbase) + (voff)[_i]), (PG8_LAS unsigned*)(lds + (bufoff) + ldsw + _i * 8192), 16, 0, 0); } while (0)
; #define PG8_LDA(dst, b, h) do { _Pragma("unroll") for (int m = 0; m < 4; ++m) _Pragma("unroll") for (int k = 0; k < 2; ++k) dst[m][k] = *(const PG8_LAS bf16x8*)(lds + PG8_SA(b, h) + aoff + m * 2048 + k * 1024); } while (0)
; #define PG8_LDB(dst, b, h) do { _Pragma("unroll") for (int n = 0; n < 2; ++n) _Pragma("unroll") for (int k = 0; k < 2; ++k) dst[n][k] = *(const PG8_LAS bf16x8*)(lds + PG8_SB(b, h) + boff + n * 2048 + k * 1024); } while (0)
; #define PG8_MMA(ai, bj, At, Bt) do { __builtin_amdgcn_s_setprio(1); _Pragma("unroll") for (int m = 0; m < 4; ++m) _Pragma("unroll") for (int n = 0; n < 2; ++n) _Pragma("unroll") for (int k = 0; k < 2; ++k) \
;         acc[ai][bj][m][n] = __builtin_amdgcn_mfma_f32_16x16x32_bf16(Bt[n][k], At[m][k], acc[ai][bj][m][n], 0, 0, 0); __builtin_amdgcn_s_setprio(0); } while (0)
; #define PG8_WAIT_V(n) asm volatile("s_waitcnt vmcnt(" #n ")" ::: "memory")
; #define PG8_WAIT_L(n) asm volatile("s_waitcnt lgkmcnt(" #n ")" ::: "memory")
; #define PG8_BAR __builtin_amdgcn_s_barrier()
; #define PG8_SCHED __builtin_amdgcn_sched_barrier(0)
; template <class Epi, class Sched, bool ALIGN_EPI = false, bool SP2 = false>
; __device__ __forceinline__ void gemm_phase(PG8_LAS unsigned char* lds, const Gemm g, const Sched& S, const Epi& E) {
;     ...
;             PG8_LDB(B0, 1, 0); PG8_LDB(B1, 1, 1); PG8_SCHED; PG8_LDA(At, 1, 0); PG8_STAGE(PG8_SA(0, 1), a2 + hstep, voffA);
;             PG8_WAIT_V(8); PG8_WAIT_L(0); PG8_BAR; PG8_MMA(0, 0, At, B0); PG8_MMA(0, 1, At, B1); PG8_BAR; PG8_SCHED;
;             PG8_LDA(At, 1, 1); PG8_STAGE(PG8_SB(1, 0), b3, voffB); PG8_STAGE(PG8_SB(1, 1), b3 + hstep, voffB); PG8_STAGE(PG8_SA(1, 0), a3, voffA);
;             PG8_WAIT_V(8); PG8_WAIT_L(0); PG8_BAR; PG8_MMA(1, 0, At, B0); PG8_MMA(1, 1, At, B1); PG8_BAR; PG8_SCHED;
;     ...
;         if constexpr (ALIGN_EPI) { if (wr == 0) PG8_BAR; }
	s_add_i32 s62, 0, 0x18000
	s_add_i32 s63, 0, 0x1c000
	v_add_u32_e32 v162, s62, v149
	v_add_u32_e32 v178, s63, v149
	ds_read_b128 v[142:145], v162
	ds_read_b128 v[154:157], v162 offset:1024
	ds_read_b128 v[158:161], v162 offset:2048
	ds_read_b128 v[162:165], v162 offset:3072
	ds_read_b128 v[166:169], v178
	ds_read_b128 v[170:173], v178 offset:1024
	ds_read_b128 v[174:177], v178 offset:2048
	ds_read_b128 v[178:181], v178 offset:3072
	s_add_u32 s36, s36, 0x100000
	s_addc_u32 s37, s37, 0
	s_mov_b32 m0, s44
	s_nop 0
	ds_read_b128 v[184:187], v153 offset:32768
	ds_read_b128 v[188:191], v153 offset:33792
	ds_read_b128 v[192:195], v153 offset:34816
	ds_read_b128 v[196:199], v153 offset:35840
	ds_read_b128 v[200:203], v153 offset:36864
	ds_read_b128 v[204:207], v153 offset:37888
	ds_read_b128 v[208:211], v153 offset:38912
	ds_read_b128 v[212:215], v153 offset:39936
	global_load_lds_dwordx4 v130, s[36:37]
	s_nop 0
	s_mov_b32 m0, s45
	s_nop 0
	global_load_lds_dwordx4 v132, s[36:37]
	s_waitcnt vmcnt(8)
	s_waitcnt lgkmcnt(0)
	s_barrier
	s_setprio 1
	s_waitcnt lgkmcnt(0)
	v_mfma_f32_16x16x32_bf16 v[126:129], v[142:145], v[184:187], v[126:129]
	v_mfma_f32_16x16x32_bf16 v[122:125], v[158:161], v[184:187], v[122:125]
	v_mfma_f32_16x16x32_bf16 v[110:113], v[142:145], v[192:195], v[110:113]
	v_mfma_f32_16x16x32_bf16 v[106:109], v[158:161], v[192:195], v[106:109]
	v_mfma_f32_16x16x32_bf16 v[94:97], v[142:145], v[200:203], v[94:97]
	v_mfma_f32_16x16x32_bf16 v[90:93], v[158:161], v[200:203], v[90:93]
	v_mfma_f32_16x16x32_bf16 v[86:89], v[142:145], v[208:211], v[86:89]
	v_mfma_f32_16x16x32_bf16 v[78:81], v[158:161], v[208:211], v[78:81]
	v_mfma_f32_16x16x32_bf16 v[126:129], v[154:157], v[188:191], v[126:129]
	v_mfma_f32_16x16x32_bf16 v[122:125], v[162:165], v[188:191], v[122:125]
	v_mfma_f32_16x16x32_bf16 v[110:113], v[154:157], v[196:199], v[110:113]
	v_mfma_f32_16x16x32_bf16 v[106:109], v[162:165], v[196:199], v[106:109]
	v_mfma_f32_16x16x32_bf16 v[94:97], v[154:157], v[204:207], v[94:97]
	v_mfma_f32_16x16x32_bf16 v[90:93], v[162:165], v[204:207], v[90:93]
	v_mfma_f32_16x16x32_bf16 v[86:89], v[154:157], v[212:215], v[86:89]
	v_mfma_f32_16x16x32_bf16 v[78:81], v[162:165], v[212:215], v[78:81]
	s_setprio 0
	s_setprio 1
	v_mfma_f32_16x16x32_bf16 v[118:121], v[166:169], v[184:187], v[118:121]
	v_mfma_f32_16x16x32_bf16 v[114:117], v[174:177], v[184:187], v[114:117]
	v_mfma_f32_16x16x32_bf16 v[102:105], v[166:169], v[192:195], v[102:105]
	v_mfma_f32_16x16x32_bf16 v[98:101], v[174:177], v[192:195], v[98:101]
	v_mfma_f32_16x16x32_bf16 v[82:85], v[166:169], v[200:203], v[82:85]
	v_mfma_f32_16x16x32_bf16 v[74:77], v[174:177], v[200:203], v[74:77]
	v_mfma_f32_16x16x32_bf16 v[70:73], v[166:169], v[208:211], v[70:73]
	v_mfma_f32_16x16x32_bf16 v[66:69], v[174:177], v[208:211], v[66:69]
	v_mfma_f32_16x16x32_bf16 v[118:121], v[170:173], v[188:191], v[118:121]
	v_mfma_f32_16x16x32_bf16 v[114:117], v[178:181], v[188:191], v[114:117]
	v_mfma_f32_16x16x32_bf16 v[102:105], v[170:173], v[196:199], v[102:105]
	v_mfma_f32_16x16x32_bf16 v[98:101], v[178:181], v[196:199], v[98:101]
	v_mfma_f32_16x16x32_bf16 v[82:85], v[170:173], v[204:207], v[82:85]
	v_mfma_f32_16x16x32_bf16 v[74:77], v[178:181], v[204:207], v[74:77]
	v_mfma_f32_16x16x32_bf16 v[70:73], v[170:173], v[212:215], v[70:73]
	v_mfma_f32_16x16x32_bf16 v[66:69], v[178:181], v[212:215], v[66:69]
	s_setprio 0
	s_barrier
	s_add_i32 s36, s62, s33
	s_add_u32 s82, s34, s12
	s_addc_u32 s83, s35, s13
	s_mov_b32 m0, s36
	ds_read_b128 v[184:187], v153 offset:49152
	ds_read_b128 v[188:191], v153 offset:50176
	ds_read_b128 v[192:195], v153 offset:51200
	ds_read_b128 v[196:199], v153 offset:52224
	ds_read_b128 v[200:203], v153 offset:53248
	ds_read_b128 v[204:207], v153 offset:54272
	ds_read_b128 v[208:211], v153 offset:55296
	ds_read_b128 v[212:215], v153 offset:56320
	global_load_lds_dwordx4 v130, s[82:83]
	s_add_i32 m0, s36, 0x2000
	s_add_u32 s34, s34, 0x100080
	s_nop 0
	s_addc_u32 s35, s35, 0
	s_add_i32 s36, s63, s33
	global_load_lds_dwordx4 v132, s[82:83]
	s_nop 0
	s_mov_b32 m0, s36
	s_nop 0
	global_load_lds_dwordx4 v130, s[34:35]
	s_nop 0
	s_add_i32 m0, s36, 0x2000
	s_nop 0
	global_load_lds_dwordx4 v132, s[34:35]
	s_nop 0
	s_mov_b32 m0, s49
	s_nop 0
	global_load_lds_dwordx4 v130, s[84:85]
	s_nop 0
	s_mov_b32 m0, s50
	s_nop 0
	global_load_lds_dwordx4 v132, s[84:85]
	s_waitcnt vmcnt(8)
	s_waitcnt lgkmcnt(0)
	s_barrier
	s_setprio 1
	s_waitcnt lgkmcnt(0)
	v_mfma_f32_16x16x32_bf16 v[62:65], v[142:145], v[184:187], v[62:65]
	v_mfma_f32_16x16x32_bf16 v[58:61], v[158:161], v[184:187], v[58:61]
	v_mfma_f32_16x16x32_bf16 v[50:53], v[142:145], v[192:195], v[50:53]
	v_mfma_f32_16x16x32_bf16 v[42:45], v[158:161], v[192:195], v[42:45]
	v_mfma_f32_16x16x32_bf16 v[34:37], v[142:145], v[200:203], v[34:37]
	v_mfma_f32_16x16x32_bf16 v[26:29], v[158:161], v[200:203], v[26:29]
	v_mfma_f32_16x16x32_bf16 v[14:17], v[142:145], v[208:211], v[14:17]
	v_mfma_f32_16x16x32_bf16 v[10:13], v[158:161], v[208:211], v[10:13]
	v_mfma_f32_16x16x32_bf16 v[62:65], v[154:157], v[188:191], v[62:65]
	v_mfma_f32_16x16x32_bf16 v[58:61], v[162:165], v[188:191], v[58:61]
	v_mfma_f32_16x16x32_bf16 v[50:53], v[154:157], v[196:199], v[50:53]
	v_mfma_f32_16x16x32_bf16 v[42:45], v[162:165], v[196:199], v[42:45]
	v_mfma_f32_16x16x32_bf16 v[34:37], v[154:157], v[204:207], v[34:37]
	v_mfma_f32_16x16x32_bf16 v[26:29], v[162:165], v[204:207], v[26:29]
	v_mfma_f32_16x16x32_bf16 v[14:17], v[154:157], v[212:215], v[14:17]
	v_mfma_f32_16x16x32_bf16 v[10:13], v[162:165], v[212:215], v[10:13]
	s_setprio 0
	s_setprio 1
	v_mfma_f32_16x16x32_bf16 v[54:57], v[166:169], v[184:187], v[54:57]
	v_mfma_f32_16x16x32_bf16 v[46:49], v[174:177], v[184:187], v[46:49]
	v_mfma_f32_16x16x32_bf16 v[38:41], v[166:169], v[192:195], v[38:41]
	v_mfma_f32_16x16x32_bf16 v[30:33], v[174:177], v[192:195], v[30:33]
	v_mfma_f32_16x16x32_bf16 v[22:25], v[166:169], v[200:203], v[22:25]
	v_mfma_f32_16x16x32_bf16 v[18:21], v[174:177], v[200:203], v[18:21]
	v_mfma_f32_16x16x32_bf16 v[6:9], v[166:169], v[208:211], v[6:9]
	v_mfma_f32_16x16x32_bf16 v[2:5], v[174:177], v[208:211], v[2:5]
	v_mfma_f32_16x16x32_bf16 v[54:57], v[170:173], v[188:191], v[54:57]
	v_mfma_f32_16x16x32_bf16 v[46:49], v[178:181], v[188:191], v[46:49]
	v_mfma_f32_16x16x32_bf16 v[38:41], v[170:173], v[196:199], v[38:41]
	v_mfma_f32_16x16x32_bf16 v[30:33], v[178:181], v[196:199], v[30:33]
	v_mfma_f32_16x16x32_bf16 v[22:25], v[170:173], v[204:207], v[22:25]
	v_mfma_f32_16x16x32_bf16 v[18:21], v[178:181], v[204:207], v[18:21]
	v_mfma_f32_16x16x32_bf16 v[6:9], v[170:173], v[212:215], v[6:9]
	v_mfma_f32_16x16x32_bf16 v[2:5], v[178:181], v[212:215], v[2:5]
	s_setprio 0
	s_barrier
	s_add_i32 s61, s61, 2
	s_add_u32 s30, s30, 0x100
	s_addc_u32 s31, s31, 0
	s_add_u32 s59, s59, 0x100
	s_addc_u32 s60, s60, 0
	s_cmp_gt_u32 s61, 61
	s_cbranch_scc0 .LBB0_707
	s_and_b64 vcc, exec, s[14:15]
	s_cbranch_vccz .LBB0_710
	s_barrier
